# speedup vs baseline: 1.0149x; 1.0149x over previous
_Z11prep_kernelPKfS0_S0_S0_S0_S0_S0_PKiPc:
	v_and_b32_e32 v18, 0x3ff, v0
	s_load_dwordx8 s[36:43], s[0:1], 0x0
	s_load_dwordx8 s[12:19], s[0:1], 0x20
	s_load_dwordx2 s[28:29], s[0:1], 0x40
	v_lshl_or_b32 v14, s2, 8, v18
	v_mov_b32_e32 v32, 0
	v_mov_b32_e32 v33, 0
	v_mov_b32_e32 v34, 0
	v_mov_b32_e32 v35, 0
	v_lshlrev_b32_e32 v36, 4, v14
	s_mov_b32 s3, 0x1e848
	v_mov_b32_e32 v1, 0x1e847
	v_cmp_gt_i32_e64 s[8:9], s3, v14
	v_mov_b32_e32 v17, 0
	v_ashrrev_i32_e32 v27, 6, v14
	v_cndmask_b32_e64 v1, v1, v14, s[8:9]
	v_lshlrev_b32_e32 v2, 1, v1
	v_ashrrev_i32_e32 v3, 31, v2
	s_waitcnt lgkmcnt(0)
	s_add_u32 s44, s28, 0x200000
	s_addc_u32 s45, s29, 0
	s_add_u32 s46, s28, 0x400000
	s_addc_u32 s47, s29, 0
	s_add_u32 s48, s28, 0x600000
	s_addc_u32 s49, s29, 0
	global_store_dwordx4 v36, v[32:35], s[28:29] sc1
	global_store_dwordx4 v36, v[32:35], s[44:45] sc1
	global_store_dwordx4 v36, v[32:35], s[46:47] sc1
	global_store_dwordx4 v36, v[32:35], s[48:49] sc1
	s_cmp_gt_u32 s2, 15
	s_cbranch_scc1 .Lprep_nz5
	s_add_u32 s50, s28, 0x800000
	s_addc_u32 s51, s29, 0
	global_store_dwordx4 v36, v[32:35], s[50:51] sc1
.Lprep_nz5:
	v_lshl_add_u64 v[10:11], v[2:3], 4, s[18:19]
	global_load_dwordx4 v[2:5], v[10:11], off offset:16
	global_load_dwordx4 v[6:9], v[10:11], off
	v_lshl_add_u32 v10, v1, 3, -1
	v_cmp_lt_i32_e32 vcc, 0, v1
	v_and_b32_e32 v28, 63, v0
	s_movk_i32 s3, 0x4000
	v_cndmask_b32_e32 v16, 0, v10, vcc
	v_lshl_add_u64 v[10:11], v[16:17], 2, s[18:19]
	global_load_dword v1, v[10:11], off
	v_min_i32_e32 v10, 0x7f, v27
	v_lshl_or_b32 v10, v10, 7, v28
	v_ashrrev_i32_e32 v11, 31, v10
	v_lshl_add_u64 v[10:11], v[10:11], 2, s[36:37]
	global_load_dword v29, v[10:11], off
	global_load_dword v26, v[10:11], off offset:256
	v_mov_b32_e32 v10, 0x3fff
	v_cmp_gt_i32_e32 vcc, s3, v14
	s_movk_i32 s3, 0x3000
	v_cmp_gt_i32_e64 s[4:5], s3, v14
	v_cndmask_b32_e32 v10, v10, v14, vcc
	v_ashrrev_i32_e32 v11, 31, v10
	v_lshl_add_u64 v[10:11], v[10:11], 2, s[12:13]
	global_load_dword v25, v[10:11], off
	v_mov_b32_e32 v10, 0x2fff
	v_cndmask_b32_e64 v10, v10, v14, s[4:5]
	v_ashrrev_i32_e32 v11, 31, v10
	v_lshl_add_u64 v[10:11], v[10:11], 2, s[14:15]
	s_movk_i32 s3, 0x1800
	global_load_dword v24, v[10:11], off
	v_mov_b32_e32 v10, 0x17ff
	v_cmp_gt_i32_e64 s[6:7], s3, v14
	s_movk_i32 s3, 0x80
	v_cmp_gt_i32_e64 s[10:11], s3, v14
	v_cndmask_b32_e64 v10, v10, v14, s[6:7]
	v_ashrrev_i32_e32 v11, 31, v10
	v_lshl_add_u64 v[10:11], v[10:11], 2, s[16:17]
	global_load_dword v23, v[10:11], off
	v_mov_b32_e32 v10, 0x7f
	v_cndmask_b32_e64 v10, v10, v14, s[10:11]
	v_ashrrev_i32_e32 v11, 31, v10
	v_lshlrev_b64 v[10:11], 2, v[10:11]
	v_lshl_add_u64 v[12:13], s[38:39], 0, v[10:11]
	global_load_dword v16, v[12:13], off
	v_lshl_add_u64 v[12:13], s[40:41], 0, v[10:11]
	v_lshl_add_u64 v[10:11], s[42:43], 0, v[10:11]
	global_load_dword v19, v[12:13], off
	global_load_dword v22, v[10:11], off
	v_lshlrev_b32_e32 v31, 2, v28
	global_load_dword v30, v31, s[38:39]
	global_load_dword v31, v31, s[38:39] offset:256
	v_ashrrev_i32_e32 v15, 31, v14
	v_mov_b32_e32 v10, 0
	s_and_saveexec_b64 s[12:13], s[8:9]
	s_cbranch_execz .LBB0_7
	s_waitcnt vmcnt(12)
	v_pk_mov_b32 v[20:21], v[2:3], v[4:5] op_sel:[1,0]
	s_waitcnt vmcnt(11)
	v_pk_mov_b32 v[12:13], v[8:9], v[2:3] op_sel:[1,0]
	v_cmp_lt_i32_e64 s[0:1], v4, v20
	v_pk_mov_b32 v[10:11], v[6:7], v[8:9] op_sel:[1,0]
	s_movk_i32 s3, 0xff
	v_cndmask_b32_e64 v20, 0, 1, s[0:1]
	v_cmp_lt_i32_e64 s[0:1], v5, v21
	v_lshlrev_b16_e32 v20, 2, v20
	s_nop 0
	v_cndmask_b32_e64 v21, 0, 1, s[0:1]
	v_cmp_lt_i32_e64 s[0:1], v3, v13
	v_lshlrev_b16_e32 v21, 3, v21
	v_or_b32_e32 v20, v21, v20
	v_cndmask_b32_e64 v13, 0, 1, s[0:1]
	v_cmp_lt_i32_e64 s[0:1], v2, v12
	v_lshlrev_b16_e32 v13, 1, v13
	s_nop 0
	v_cndmask_b32_e64 v12, 0, 1, s[0:1]
	v_cmp_lt_i32_e64 s[0:1], v8, v10
	v_or_b32_e32 v12, v12, v13
	v_bitop3_b16 v12, v12, v20, 3 bitop3:0xec
	v_cndmask_b32_e64 v10, 0, 1, s[0:1]
	v_cmp_lt_i32_e64 s[0:1], v9, v11
	v_lshlrev_b16_e32 v10, 2, v10
	v_lshlrev_b16_e32 v12, 4, v12
	v_cndmask_b32_e64 v11, 0, 1, s[0:1]
	v_lshlrev_b16_e32 v11, 3, v11
	v_cmp_lt_i32_e64 s[0:1], v7, v6
	v_or_b32_e32 v10, v11, v10
	s_nop 0
	v_cndmask_b32_e64 v11, 0, 1, s[0:1]
	s_waitcnt vmcnt(10)
	v_cmp_lt_i32_e64 s[0:1], v6, v1
	v_lshlrev_b16_e32 v11, 1, v11
	v_or_b32_e32 v6, v7, v6
	v_cndmask_b32_e64 v1, 0, 1, s[0:1]
	v_bitop3_b16 v1, v1, 3, v11 bitop3:0xc8
	v_or3_b32 v6, v6, v8, v9
	v_bitop3_b16 v1, v1, 15, v10 bitop3:0xc8
	v_or3_b32 v2, v6, v2, v3
	v_or3_b32 v2, v2, v4, v5
	s_movk_i32 s0, 0x3fff
	v_bitop3_b16 v1, v1, s3, v12 bitop3:0xc8
	v_cmp_lt_u32_e64 s[0:1], s0, v2
	v_cmp_ne_u16_e64 s[8:9], 0, v1
	s_or_b64 s[0:1], s[8:9], s[0:1]
	v_cndmask_b32_e64 v10, 0, 1, s[0:1]
.LBB0_7:
	s_or_b64 exec, exec, s[12:13]
	s_waitcnt vmcnt(10)
	v_cmp_ne_u32_e64 s[8:9], 0, v10
	v_lshrrev_b32_e32 v0, 6, v18
	v_lshlrev_b32_e32 v0, 2, v0
	s_cmp_lg_u64 s[8:9], 0
	s_cselect_b32 s3, 1, 0
	v_mov_b32_e32 v1, s3
	ds_write_b32 v0, v1
	s_waitcnt lgkmcnt(0)
	s_barrier
	v_cmp_eq_u32_e64 s[0:1], 0, v18
	s_and_saveexec_b64 s[8:9], s[0:1]
	s_cbranch_execz .LBB0_16
	v_mov_b32_e32 v0, 0
	ds_read_b128 v[4:7], v0
	s_mov_b32 s3, 0
	s_lshl_b64 s[0:1], s[2:3], 2
	s_add_u32 s0, s28, s0
	s_addc_u32 s1, s29, s1
	v_mov_b32_e32 v0, 0x829000
	s_waitcnt lgkmcnt(0)
	v_or_b32_e32 v1, v4, v5
	v_or3_b32 v1, v1, v6, v7
	global_store_dword v0, v1, s[0:1] offset:2048

.LBB0_22:
	s_waitcnt vmcnt(8)
	v_add_f32_e32 v0, v29, v26
	s_nop 1
	v_add_f32_dpp v0, v0, v0 quad_perm:[1,0,3,2] row_mask:0xf bank_mask:0xf bound_ctrl:1
	s_nop 1
	v_add_f32_dpp v0, v0, v0 quad_perm:[2,3,0,1] row_mask:0xf bank_mask:0xf bound_ctrl:1
	s_nop 1
	v_add_f32_dpp v0, v0, v0 row_half_mirror row_mask:0xf bank_mask:0xf bound_ctrl:1
	s_nop 1
	v_add_f32_dpp v0, v0, v0 row_mirror row_mask:0xf bank_mask:0xf bound_ctrl:1
	s_nop 1
	v_readlane_b32 s44, v0, 0
	v_readlane_b32 s45, v0, 16
	v_readlane_b32 s46, v0, 32
	v_readlane_b32 s47, v0, 48
	s_mov_b32 s8, 0x7ffff8
	v_bfe_u32 v2, v14, 6, 3
	v_lshrrev_b32_e32 v3, 8, v14
	s_add_u32 s0, s28, 0x810000
	s_addc_u32 s1, s29, 0
	v_mov_b32_e32 v4, s44
	v_add_f32_e32 v4, s45, v4
	v_add_f32_e32 v4, s46, v4
	v_add_f32_e32 v4, s47, v4
	v_lshrrev_b32_e32 v0, 4, v28
	v_and_or_b32 v0, v3, s8, v0
	v_lshlrev_b32_e32 v3, 1, v27
	v_and_b32_e32 v1, 15, v18
	v_lshlrev_b32_e32 v0, 6, v0
	v_and_b32_e32 v3, 48, v3
	v_or3_b32 v0, v0, v1, v3
	v_lshl_or_b32 v0, v0, 3, v2
	v_ashrrev_i32_e32 v1, 31, v0
	v_fmac_f32_e32 v29, 0xbc000000, v4
	v_lshl_add_u64 v[2:3], v[0:1], 1, s[0:1]
	v_or_b32_e32 v0, 0x800, v0
	v_cvt_pk_bf16_f32 v5, v29, s0
	v_fmac_f32_e32 v26, 0xbc000000, v4
	v_ashrrev_i32_e32 v1, 31, v0
	global_store_short v[2:3], v5, off
	v_cvt_pk_bf16_f32 v2, v26, s0
	v_lshl_add_u64 v[0:1], v[0:1], 1, s[0:1]
	global_store_short v[0:1], v2, off
	s_or_b64 exec, exec, s[2:3]
	s_and_saveexec_b64 s[0:1], vcc
	s_cbranch_execz .LBB0_18
.LBB0_23:
	v_lshrrev_b32_e32 v0, 25, v15
	v_add_u32_e32 v0, v14, v0
	v_ashrrev_i32_e32 v1, 7, v0
	v_and_b32_e32 v0, 0xffffff80, v0
	v_sub_u32_e32 v0, v14, v0
	v_lshrrev_b32_e32 v5, 2, v1
	v_and_b32_e32 v3, 15, v0
	v_and_b32_e32 v5, 4, v5
	v_lshrrev_b32_e32 v0, 2, v0
	v_lshrrev_b32_e32 v4, 5, v1
	v_and_or_b32 v5, v1, 3, v5
	v_and_b32_e32 v0, 0x7ffffc, v0
	v_lshlrev_b32_e32 v1, 2, v1
	v_add_lshl_u32 v0, v0, v4, 6
	v_and_b32_e32 v1, 48, v1
	v_or3_b32 v0, v0, v3, v1
	v_lshl_or_b32 v0, v0, 3, v5
	v_ashrrev_i32_e32 v1, 31, v0
	v_lshl_add_u64 v[0:1], v[0:1], 1, s[28:29]
	v_add_co_u32_e32 v0, vcc, 0x818000, v0
	s_waitcnt vmcnt(7)
	v_cvt_pk_bf16_f32 v2, v25, s0
	v_addc_co_u32_e32 v1, vcc, 0, v1, vcc
	global_store_short v[0:1], v2, off offset:2048
	s_or_b64 exec, exec, s[0:1]
	s_and_saveexec_b64 s[0:1], s[4:5]
	s_cbranch_execz .LBB0_19
.LBB0_24:
	s_mov_b32 s2, 0x2aaaaaab
	v_mul_hi_i32 v0, v14, s2
	v_lshrrev_b32_e32 v1, 31, v0
	v_ashrrev_i32_e32 v0, 4, v0
	v_add_u32_e32 v0, v0, v1
	s_movk_i32 s2, 0x60
	v_mul_lo_u32 v1, v0, s2
	v_sub_u32_e32 v1, v14, v1
	v_lshrrev_b32_e32 v5, 2, v0
	v_and_b32_e32 v3, 15, v1
	v_and_b32_e32 v5, 4, v5
	v_lshrrev_b32_e32 v1, 2, v1
	v_lshrrev_b32_e32 v4, 5, v0
	v_and_or_b32 v5, v0, 3, v5
	v_and_b32_e32 v1, 0x7ffffc, v1
	v_lshlrev_b32_e32 v0, 2, v0
	v_add_lshl_u32 v1, v1, v4, 6
	v_and_b32_e32 v0, 48, v0
	v_or3_b32 v0, v1, v3, v0
	v_lshl_or_b32 v0, v0, 3, v5
	v_ashrrev_i32_e32 v1, 31, v0
	v_lshl_add_u64 v[0:1], v[0:1], 1, s[28:29]
	v_add_co_u32_e32 v0, vcc, 0x820000, v0
	s_waitcnt vmcnt(6)
	v_cvt_pk_bf16_f32 v2, v24, s0
	v_addc_co_u32_e32 v1, vcc, 0, v1, vcc
	global_store_short v[0:1], v2, off offset:2048
	s_or_b64 exec, exec, s[0:1]
	s_and_saveexec_b64 s[0:1], s[6:7]
	s_cbranch_execz .LBB0_20
.LBB0_25:
	v_lshrrev_b32_e32 v0, 26, v15
	v_add_u32_e32 v0, v14, v0
	v_ashrrev_i32_e32 v1, 6, v0
	v_and_b32_e32 v0, 0xffffffc0, v0
	v_sub_u32_e32 v0, v14, v0
	v_lshrrev_b32_e32 v5, 2, v1
	v_lshrrev_b32_e32 v3, 4, v0
	v_and_b32_e32 v5, 4, v5
	v_lshrrev_b32_e32 v4, 5, v1
	v_and_or_b32 v5, v1, 3, v5
	v_lshl_add_u32 v3, v3, 1, v3
	v_lshlrev_b32_e32 v1, 2, v1
	v_and_b32_e32 v0, 15, v0
	v_add_lshl_u32 v3, v3, v4, 6
	v_and_b32_e32 v1, 48, v1
	v_or3_b32 v0, v3, v0, v1
	v_lshl_or_b32 v0, v0, 3, v5
	v_ashrrev_i32_e32 v1, 31, v0
	v_lshl_add_u64 v[0:1], v[0:1], 1, s[28:29]
	v_add_co_u32_e32 v0, vcc, 0x826000, v0
	s_waitcnt vmcnt(5)
	v_cvt_pk_bf16_f32 v2, v23, s0
	v_addc_co_u32_e32 v1, vcc, 0, v1, vcc
	global_store_short v[0:1], v2, off offset:2048
	s_or_b64 exec, exec, s[0:1]
	s_and_saveexec_b64 s[0:1], s[10:11]
	s_cbranch_execz .LBB0_21
.LBB0_26:
	s_waitcnt vmcnt(0)
	v_add_f32_e32 v0, v30, v31
	s_nop 1
	v_add_f32_dpp v0, v0, v0 quad_perm:[1,0,3,2] row_mask:0xf bank_mask:0xf bound_ctrl:1
	s_nop 1
	v_add_f32_dpp v0, v0, v0 quad_perm:[2,3,0,1] row_mask:0xf bank_mask:0xf bound_ctrl:1
	s_nop 1
	v_add_f32_dpp v0, v0, v0 row_half_mirror row_mask:0xf bank_mask:0xf bound_ctrl:1
	s_nop 1
	v_add_f32_dpp v0, v0, v0 row_mirror row_mask:0xf bank_mask:0xf bound_ctrl:1
	s_nop 1
	v_readlane_b32 s44, v0, 0
	v_readlane_b32 s45, v0, 16
	v_readlane_b32 s46, v0, 32
	v_readlane_b32 s47, v0, 48
	v_mov_b32_e32 v17, s44
	v_add_f32_e32 v17, s45, v17
	v_add_f32_e32 v17, s46, v17
	v_add_f32_e32 v17, s47, v17
	v_lshl_add_u64 v[0:1], v[14:15], 2, s[28:29]
	s_mov_b64 s[0:1], 0x818000
	v_lshl_add_u64 v[2:3], v[0:1], 0, s[0:1]
	v_add_co_u32_e32 v0, vcc, 0x818000, v0
	v_fmamk_f32 v6, v17, 0xbc000000, v16
	v_addc_co_u32_e32 v1, vcc, 0, v1, vcc
	v_mul_f32_e32 v4, 0x4038aa3b, v22
	v_mul_f32_e32 v5, 0x4038aa3b, v19
	global_store_dword v[0:1], v6, off
	global_store_dword v[2:3], v5, off offset:512
	global_store_dword v[2:3], v4, off offset:1024
	s_endpgm

	.amdhsa_kernel _Z11prep_kernelPKfS0_S0_S0_S0_S0_S0_PKiPc
		.amdhsa_group_segment_fixed_size 256
		.amdhsa_private_segment_fixed_size 0
		.amdhsa_kernarg_size 328
		.amdhsa_user_sgpr_count 2
		.amdhsa_user_sgpr_dispatch_ptr 0
		.amdhsa_user_sgpr_queue_ptr 0
		.amdhsa_user_sgpr_kernarg_segment_ptr 1
		.amdhsa_user_sgpr_dispatch_id 0
		.amdhsa_user_sgpr_kernarg_preload_length 0
		.amdhsa_user_sgpr_kernarg_preload_offset 0
		.amdhsa_user_sgpr_private_segment_size 0
		.amdhsa_uses_dynamic_stack 0
		.amdhsa_enable_private_segment 0
		.amdhsa_system_sgpr_workgroup_id_x 1
		.amdhsa_system_sgpr_workgroup_id_y 0
		.amdhsa_system_sgpr_workgroup_id_z 0
		.amdhsa_system_sgpr_workgroup_info 0
		.amdhsa_system_vgpr_workitem_id 2
		.amdhsa_next_free_vgpr 37
		.amdhsa_next_free_sgpr 52
		.amdhsa_accum_offset 40
		.amdhsa_reserve_vcc 1
		.amdhsa_float_round_mode_32 0
		.amdhsa_float_round_mode_16_64 0
		.amdhsa_float_denorm_mode_32 3
		.amdhsa_float_denorm_mode_16_64 3
		.amdhsa_dx10_clamp 1
		.amdhsa_ieee_mode 1
		.amdhsa_fp16_overflow 0
		.amdhsa_tg_split 0
		.amdhsa_exception_fp_ieee_invalid_op 0
		.amdhsa_exception_fp_denorm_src 0
		.amdhsa_exception_fp_ieee_div_zero 0
		.amdhsa_exception_fp_ieee_overflow 0
		.amdhsa_exception_fp_ieee_underflow 0
		.amdhsa_exception_fp_ieee_inexact 0
		.amdhsa_exception_int_div_zero 0
	.end_amdhsa_kernel

.LBB1_12:
	s_mov_b32 s0, s44
	s_add_i32 s44, s44, 1
	s_cmp_ge_u32 s44, s42
	s_cselect_b64 s[22:23], -1, 0
	s_cmp_lt_u32 s44, s42
	s_cselect_b32 s2, s44, s0
	s_waitcnt vmcnt(0)
	s_lshl_b32 s0, s2, 4
	s_mov_b32 s1, s17
	s_mov_b32 m0, s43
	ds_read_b128 v[76:79], v119 offset:32768
	ds_read_b128 v[80:83], v119 offset:36864
	ds_read_b128 v[84:87], v120 offset:32768
	ds_read_b128 v[88:91], v120 offset:36864
	ds_read_b128 v[92:95], v121
	ds_read_b128 v[96:99], v121 offset:4096
	ds_read_b128 v[128:131], v122
	ds_read_b128 v[132:135], v122 offset:4096
	ds_read_b128 v[72:75], v123
	s_waitcnt lgkmcnt(0)
	v_lshl_add_u64 v[70:71], s[0:1], 2, v[2:3]
	global_load_lds_dword v[70:71], off
	s_waitcnt lgkmcnt(0)
	v_cvt_pk_bf16_f32 v76, v76, v77
	v_cvt_pk_bf16_f32 v77, v78, v79
	v_cvt_pk_bf16_f32 v78, v84, v85
	v_cvt_pk_bf16_f32 v79, v86, v87
	v_cvt_pk_bf16_f32 v84, v92, v93
	v_cvt_pk_bf16_f32 v85, v94, v95
	v_cvt_pk_bf16_f32 v86, v128, v129
	v_cvt_pk_bf16_f32 v87, v130, v131
	v_cvt_pk_bf16_f32 v80, v80, v81
	v_cvt_pk_bf16_f32 v81, v82, v83
	v_cvt_pk_bf16_f32 v82, v88, v89
	v_cvt_pk_bf16_f32 v83, v90, v91
	v_cvt_pk_bf16_f32 v128, v96, v97
	v_cvt_pk_bf16_f32 v129, v98, v99
	v_cvt_pk_bf16_f32 v130, v132, v133
	v_cvt_pk_bf16_f32 v131, v134, v135
	ds_read_b128 v[88:91], v115
	ds_read_b128 v[92:95], v115 offset:1024
	ds_read_b128 v[96:99], v115 offset:2048
	ds_read_b128 v[132:135], v115 offset:3072
	s_lshl_b32 s0, s2, 13
	s_waitcnt lgkmcnt(0)
	v_mfma_f32_16x16x32_bf16 v[88:91], v[76:79], v[88:91], v[36:39]
	v_mfma_f32_16x16x32_bf16 v[96:99], v[76:79], v[96:99], v[44:47]
	v_mfma_f32_16x16x32_bf16 v[92:95], v[76:79], v[92:95], v[40:43]
	v_mfma_f32_16x16x32_bf16 v[132:135], v[76:79], v[132:135], v[48:51]
	s_mov_b32 m0, s47
	s_nop 0
	buffer_load_dwordx4 v113, s[12:15], s0 offen nt lds
	ds_read_b128 v[136:139], v115 offset:4096
	ds_read_b128 v[140:143], v115 offset:5120
	ds_read_b128 v[144:147], v115 offset:6144
	ds_read_b128 v[148:151], v115 offset:7168
	s_waitcnt lgkmcnt(0)
	v_mfma_f32_16x16x32_bf16 v[136:139], v[76:79], v[136:139], v[52:55]
	v_mfma_f32_16x16x32_bf16 v[140:143], v[76:79], v[140:143], v[56:59]
	v_mfma_f32_16x16x32_bf16 v[144:147], v[76:79], v[144:147], v[60:63]
	v_mfma_f32_16x16x32_bf16 v[76:79], v[76:79], v[148:151], v[64:67]
	s_or_b32 s1, s0, 0x800
	s_mov_b32 m0, s48
	s_nop 0
	buffer_load_dwordx4 v113, s[12:15], s1 offen nt lds
	ds_read_b128 v[148:151], v115 offset:8192
	ds_read_b128 v[152:155], v115 offset:9216
	s_waitcnt lgkmcnt(0)
	v_mfma_f32_16x16x32_bf16 v[88:91], v[84:87], v[148:151], v[88:91]
	v_mfma_f32_16x16x32_bf16 v[92:95], v[84:87], v[152:155], v[92:95]
	ds_read_b128 v[148:151], v115 offset:10240
	ds_read_b128 v[152:155], v115 offset:11264
	s_waitcnt lgkmcnt(0)
	v_mfma_f32_16x16x32_bf16 v[96:99], v[84:87], v[148:151], v[96:99]
	v_mfma_f32_16x16x32_bf16 v[132:135], v[84:87], v[152:155], v[132:135]
	s_or_b32 s1, s0, 0x1000
	s_mov_b32 m0, s49
	s_nop 0
	buffer_load_dwordx4 v113, s[12:15], s1 offen nt lds
	ds_read_b128 v[148:151], v115 offset:12288
	ds_read_b128 v[152:155], v115 offset:13312
	s_waitcnt lgkmcnt(0)
	v_mfma_f32_16x16x32_bf16 v[136:139], v[84:87], v[148:151], v[136:139]
	v_mfma_f32_16x16x32_bf16 v[140:143], v[84:87], v[152:155], v[140:143]
	ds_read_b128 v[148:151], v115 offset:14336
	ds_read_b128 v[152:155], v115 offset:15360
	s_waitcnt lgkmcnt(0)
	v_mfma_f32_16x16x32_bf16 v[76:79], v[84:87], v[152:155], v[76:79]
	v_mfma_f32_16x16x32_bf16 v[144:147], v[84:87], v[148:151], v[144:147]
	s_or_b32 s1, s0, 0x1800
	s_mov_b32 m0, s50
	s_nop 0
	buffer_load_dwordx4 v113, s[12:15], s1 offen nt lds
	ds_read_b128 v[84:87], v115 offset:16384
	ds_read_b128 v[148:151], v115 offset:17408
	s_or_b32 s1, s0, 0x100
	s_waitcnt lgkmcnt(0)
	v_mfma_f32_16x16x32_bf16 v[84:87], v[80:83], v[84:87], v[88:91]
	v_mfma_f32_16x16x32_bf16 v[88:91], v[80:83], v[148:151], v[92:95]
	s_nop 2
	ds_read_b128 v[92:95], v115 offset:18432
	ds_read_b128 v[148:151], v115 offset:19456
	s_waitcnt lgkmcnt(0)
	v_mfma_f32_16x16x32_bf16 v[92:95], v[80:83], v[92:95], v[96:99]
	v_mfma_f32_16x16x32_bf16 v[132:135], v[80:83], v[148:151], v[132:135]
	s_mov_b32 m0, s51
	s_nop 0
	buffer_load_dwordx4 v113, s[12:15], s1 offen nt lds
	ds_read_b128 v[96:99], v115 offset:20480
	ds_read_b128 v[148:151], v115 offset:21504
	s_waitcnt lgkmcnt(0)
	v_mfma_f32_16x16x32_bf16 v[136:139], v[80:83], v[96:99], v[136:139]
	v_mfma_f32_16x16x32_bf16 v[140:143], v[80:83], v[148:151], v[140:143]
	ds_read_b128 v[96:99], v115 offset:22528
	ds_read_b128 v[148:151], v115 offset:23552
	s_waitcnt lgkmcnt(0)
	v_mfma_f32_16x16x32_bf16 v[76:79], v[80:83], v[148:151], v[76:79]
	v_mfma_f32_16x16x32_bf16 v[144:147], v[80:83], v[96:99], v[144:147]
	s_or_b32 s1, s0, 0x900
	s_mov_b32 m0, s52
	s_nop 0
	buffer_load_dwordx4 v113, s[12:15], s1 offen nt lds
	ds_read_b128 v[80:83], v115 offset:24576
	ds_read_b128 v[96:99], v115 offset:25600
	s_waitcnt lgkmcnt(0)
	v_mfma_f32_16x16x32_bf16 v[148:151], v[128:131], v[80:83], v[84:87]
	ds_read_b128 v[80:83], v115 offset:26624
	s_nop 1
	ds_read_b128 v[84:87], v115 offset:27648
	v_mfma_f32_16x16x32_bf16 v[152:155], v[128:131], v[96:99], v[88:91]
	s_waitcnt lgkmcnt(0)
	v_mfma_f32_16x16x32_bf16 v[96:99], v[128:131], v[80:83], v[92:95]
	v_mfma_f32_16x16x32_bf16 v[92:95], v[128:131], v[84:87], v[132:135]
	s_or_b32 s1, s0, 0x1100
	s_mov_b32 m0, s53
	s_nop 0
	buffer_load_dwordx4 v113, s[12:15], s1 offen nt lds
	ds_read_b128 v[80:83], v115 offset:28672
	ds_read_b128 v[84:87], v115 offset:29696
	s_waitcnt lgkmcnt(0)
	v_mfma_f32_16x16x32_bf16 v[88:91], v[128:131], v[80:83], v[136:139]
	ds_read_b128 v[80:83], v115 offset:30720
	ds_read_b128 v[132:135], v115 offset:31744
	v_mfma_f32_16x16x32_bf16 v[84:87], v[128:131], v[84:87], v[140:143]
	s_waitcnt lgkmcnt(0)
	v_mfma_f32_16x16x32_bf16 v[76:79], v[128:131], v[132:135], v[76:79]
	v_mfma_f32_16x16x32_bf16 v[80:83], v[128:131], v[80:83], v[144:147]
	s_or_b32 s0, s0, 0x1900
	s_mov_b32 m0, s54
	s_nop 0
	buffer_load_dwordx4 v113, s[12:15], s0 offen nt lds
	v_fma_f32 v70, v149, v149, 0
	v_fmac_f32_e32 v70, v153, v153
	v_fmac_f32_e32 v70, v97, v97
	v_fmac_f32_e32 v70, v93, v93
	v_fmac_f32_e32 v70, v89, v89
	v_fmac_f32_e32 v70, v85, v85
	v_fmac_f32_e32 v70, v81, v81
	v_fmac_f32_e32 v70, v77, v77
	v_fma_f32 v68, v148, v148, 0
	v_fmac_f32_e32 v68, v152, v152
	v_add_f32_dpp v70, v70, v70 quad_perm:[1,0,3,2] row_mask:0xf bank_mask:0xf bound_ctrl:1
	v_fmac_f32_e32 v68, v96, v96
	v_fmac_f32_e32 v68, v92, v92
	v_add_f32_dpp v70, v70, v70 quad_perm:[2,3,0,1] row_mask:0xf bank_mask:0xf bound_ctrl:1
	v_fmac_f32_e32 v68, v88, v88
	v_fmac_f32_e32 v68, v84, v84
	v_add_f32_dpp v70, v70, v70 row_half_mirror row_mask:0xf bank_mask:0xf bound_ctrl:1
	v_fmac_f32_e32 v68, v80, v80
	v_fmac_f32_e32 v68, v76, v76
	v_add_f32_dpp v70, v70, v70 row_mirror row_mask:0xf bank_mask:0xf bound_ctrl:1
	v_fmamk_f32 v70, v70, 0x3c000000, v124
	v_rsq_f32_e32 v127, v70
	v_fma_f32 v70, v150, v150, 0
	v_fmac_f32_e32 v70, v154, v154
	v_fmac_f32_e32 v70, v98, v98
	v_fmac_f32_e32 v70, v94, v94
	v_fmac_f32_e32 v70, v90, v90
	v_fmac_f32_e32 v70, v86, v86
	v_fmac_f32_e32 v70, v82, v82
	v_fmac_f32_e32 v70, v78, v78
	v_add_f32_dpp v68, v68, v68 quad_perm:[1,0,3,2] row_mask:0xf bank_mask:0xf bound_ctrl:1
	v_mul_f32_e32 v131, v127, v149
	v_add_f32_dpp v70, v70, v70 quad_perm:[1,0,3,2] row_mask:0xf bank_mask:0xf bound_ctrl:1
	v_add_f32_dpp v68, v68, v68 quad_perm:[2,3,0,1] row_mask:0xf bank_mask:0xf bound_ctrl:1
	v_mul_f32_e32 v81, v127, v81
	v_add_f32_dpp v70, v70, v70 quad_perm:[2,3,0,1] row_mask:0xf bank_mask:0xf bound_ctrl:1
	v_add_f32_dpp v68, v68, v68 row_half_mirror row_mask:0xf bank_mask:0xf bound_ctrl:1
	v_cmp_gt_u32_e64 s[0:1], s55, v72
	v_add_f32_dpp v70, v70, v70 row_half_mirror row_mask:0xf bank_mask:0xf bound_ctrl:1
	v_add_f32_dpp v68, v68, v68 row_mirror row_mask:0xf bank_mask:0xf bound_ctrl:1
	v_fmamk_f32 v68, v68, 0x3c000000, v124
	v_add_f32_dpp v70, v70, v70 row_mirror row_mask:0xf bank_mask:0xf bound_ctrl:1
	v_fmamk_f32 v70, v70, 0x3c000000, v124
	v_rsq_f32_e32 v130, v70
	v_fma_f32 v70, v151, v151, 0
	v_fmac_f32_e32 v70, v155, v155
	v_fmac_f32_e32 v70, v99, v99
	v_fmac_f32_e32 v70, v95, v95
	v_fmac_f32_e32 v70, v91, v91
	v_fmac_f32_e32 v70, v87, v87
	v_fmac_f32_e32 v70, v83, v83
	v_fmac_f32_e32 v70, v79, v79
	v_rsq_f32_e32 v68, v68
	v_mul_f32_e32 v98, v130, v98
	v_add_f32_dpp v70, v70, v70 quad_perm:[1,0,3,2] row_mask:0xf bank_mask:0xf bound_ctrl:1
	v_mul_f32_e32 v90, v130, v90
	v_mul_f32_e32 v111, v68, v148
	v_add_f32_dpp v110, v70, v70 quad_perm:[2,3,0,1] row_mask:0xf bank_mask:0xf bound_ctrl:1
	ds_read2_b32 v[70:71], v114 offset0:128 offset1:144
	ds_read2_b32 v[128:129], v125 offset1:16
	v_add_f32_dpp v110, v110, v110 row_half_mirror row_mask:0xf bank_mask:0xf bound_ctrl:1
	v_mul_f32_e32 v96, v68, v96
	v_mul_f32_e32 v92, v68, v92
	v_add_f32_dpp v110, v110, v110 row_mirror row_mask:0xf bank_mask:0xf bound_ctrl:1
	v_fmamk_f32 v110, v110, 0x3c000000, v124
	s_waitcnt lgkmcnt(0)
	v_fma_f32 v111, v111, v70, v128
	v_fma_f32 v131, v131, v70, v128
	v_exp_f32_e32 v111, v111
	v_exp_f32_e32 v131, v131
	v_rsq_f32_e32 v132, v110
	v_mul_f32_e32 v88, v68, v88
	v_add_f32_e32 v110, 1.0, v111
	v_add_f32_e32 v111, 1.0, v131
	v_mul_f32_e32 v131, v130, v150
	v_mul_f32_e32 v133, v132, v151
	v_fma_f32 v131, v131, v70, v128
	v_fma_f32 v70, v133, v70, v128
	v_exp_f32_e32 v131, v131
	v_exp_f32_e32 v70, v70
	v_rcp_f32_e32 v110, v110
	v_rcp_f32_e32 v111, v111
	v_add_f32_e32 v128, 1.0, v131
	v_add_f32_e32 v70, 1.0, v70
	v_rcp_f32_e32 v128, v128
	v_rcp_f32_e32 v70, v70
	v_mul_f32_e32 v131, v68, v152
	v_fma_f32 v131, v131, v71, v129
	v_cvt_pk_bf16_f32 v110, v110, v111
	v_cvt_pk_bf16_f32 v111, v128, v70
	v_mul_f32_e32 v128, v127, v153
	v_exp_f32_e32 v131, v131
	v_fma_f32 v128, v128, v71, v129
	v_exp_f32_e32 v128, v128
	v_mul_f32_e32 v99, v132, v99
	v_add_f32_e32 v70, 1.0, v131
	v_rcp_f32_e32 v133, v70
	v_add_f32_e32 v70, 1.0, v128
	v_mul_f32_e32 v131, v130, v154
	v_rcp_f32_e32 v134, v70
	v_mul_f32_e32 v70, v132, v155
	v_fma_f32 v131, v131, v71, v129
	v_fmac_f32_e32 v129, v70, v71
	v_exp_f32_e32 v135, v129
	ds_read2_b32 v[70:71], v114 offset0:160 offset1:176
	ds_read2_b32 v[128:129], v125 offset0:32 offset1:48
	v_exp_f32_e32 v131, v131
	v_mul_f32_e32 v91, v132, v91
	v_add_f32_e32 v135, 1.0, v135
	v_rcp_f32_e32 v135, v135
	s_waitcnt lgkmcnt(0)
	v_fma_f32 v96, v96, v70, v128
	v_exp_f32_e32 v136, v96
	v_mul_f32_e32 v96, v127, v97
	v_fma_f32 v96, v96, v70, v128
	v_exp_f32_e32 v97, v96
	v_fma_f32 v98, v98, v70, v128
	v_fma_f32 v70, v99, v70, v128
	v_exp_f32_e32 v98, v98
	v_exp_f32_e32 v70, v70
	v_add_f32_e32 v97, 1.0, v97
	v_cvt_pk_bf16_f32 v96, v133, v134
	v_add_f32_e32 v133, 1.0, v136
	v_rcp_f32_e32 v99, v97
	v_add_f32_e32 v97, 1.0, v98
	v_add_f32_e32 v70, 1.0, v70
	v_fma_f32 v92, v92, v71, v129
	v_rcp_f32_e32 v133, v133
	v_rcp_f32_e32 v128, v97
	v_rcp_f32_e32 v70, v70
	v_exp_f32_e32 v92, v92
	v_cvt_pk_bf16_f32 v98, v133, v99
	v_add_f32_e32 v131, 1.0, v131
	v_cvt_pk_bf16_f32 v99, v128, v70
	v_add_f32_e32 v70, 1.0, v92
	v_mul_f32_e32 v92, v127, v93
	v_fma_f32 v92, v92, v71, v129
	v_exp_f32_e32 v92, v92
	v_mul_f32_e32 v93, v130, v94
	v_fma_f32 v93, v93, v71, v129
	v_rcp_f32_e32 v131, v131
	v_exp_f32_e32 v93, v93
	v_rcp_f32_e32 v94, v70
	v_add_f32_e32 v70, 1.0, v92
	v_rcp_f32_e32 v128, v70
	v_mul_f32_e32 v70, v132, v95
	v_cvt_pk_bf16_f32 v97, v131, v135
	v_add_f32_e32 v131, 1.0, v93
	v_fmac_f32_e32 v129, v70, v71
	ds_read2_b32 v[70:71], v114 offset0:192 offset1:208
	ds_read2_b32 v[92:93], v125 offset0:64 offset1:80
	v_exp_f32_e32 v95, v129
	v_rcp_f32_e32 v129, v131
	v_mul_f32_e32 v84, v68, v84
	v_mul_f32_e32 v80, v68, v80
	s_waitcnt lgkmcnt(0)
	v_fma_f32 v88, v88, v70, v92
	v_exp_f32_e32 v131, v88
	v_mul_f32_e32 v88, v127, v89
	v_fma_f32 v88, v88, v70, v92
	v_exp_f32_e32 v89, v88
	v_fma_f32 v90, v90, v70, v92
	v_fma_f32 v70, v91, v70, v92
	v_exp_f32_e32 v90, v90
	v_exp_f32_e32 v70, v70
	v_add_f32_e32 v89, 1.0, v89
	v_cvt_pk_bf16_f32 v88, v94, v128
	v_add_f32_e32 v94, 1.0, v131
	v_rcp_f32_e32 v91, v89
	v_add_f32_e32 v89, 1.0, v90
	v_add_f32_e32 v70, 1.0, v70
	v_fma_f32 v84, v84, v71, v93
	v_rcp_f32_e32 v94, v94
	v_rcp_f32_e32 v92, v89
	v_rcp_f32_e32 v70, v70
	v_exp_f32_e32 v84, v84
	v_cvt_pk_bf16_f32 v90, v94, v91
	v_mul_f32_e32 v68, v68, v76
	v_cvt_pk_bf16_f32 v91, v92, v70
	v_add_f32_e32 v70, 1.0, v84
	v_mul_f32_e32 v84, v127, v85
	v_fma_f32 v84, v84, v71, v93
	v_mul_f32_e32 v85, v130, v86
	v_exp_f32_e32 v84, v84
	v_fma_f32 v85, v85, v71, v93
	v_exp_f32_e32 v85, v85
	v_rcp_f32_e32 v92, v70
	v_add_f32_e32 v70, 1.0, v84
	v_rcp_f32_e32 v84, v70
	v_add_f32_e32 v70, 1.0, v85
	v_mul_f32_e32 v85, v132, v87
	v_fmac_f32_e32 v93, v85, v71
	v_exp_f32_e32 v85, v93
	v_rcp_f32_e32 v93, v70
	ds_read2_b32 v[70:71], v114 offset0:224 offset1:240
	ds_read2_b32 v[86:87], v125 offset0:96 offset1:112
	v_mul_f32_e32 v76, v127, v77
	v_mul_f32_e32 v82, v130, v82
	v_mul_f32_e32 v83, v132, v83
	v_mul_f32_e32 v77, v130, v78
	s_waitcnt lgkmcnt(0)
	v_fma_f32 v76, v76, v71, v87
	v_mul_f32_e32 v78, v132, v79
	v_fma_f32 v80, v80, v70, v86
	v_fma_f32 v81, v81, v70, v86
	v_fma_f32 v82, v82, v70, v86
	v_fma_f32 v70, v83, v70, v86
	v_fma_f32 v68, v68, v71, v87
	v_exp_f32_e32 v76, v76
	v_fma_f32 v77, v77, v71, v87
	v_fmac_f32_e32 v87, v78, v71
	v_exp_f32_e32 v82, v82
	v_exp_f32_e32 v70, v70
	v_exp_f32_e32 v68, v68
	v_exp_f32_e32 v77, v77
	v_exp_f32_e32 v71, v87
	v_add_f32_e32 v76, 1.0, v76
	v_add_f32_e32 v82, 1.0, v82
	v_add_f32_e32 v70, 1.0, v70
	v_add_f32_e32 v68, 1.0, v68
	v_rcp_f32_e32 v78, v76
	v_add_f32_e32 v76, 1.0, v77
	v_add_f32_e32 v71, 1.0, v71
	v_rcp_f32_e32 v82, v82
	v_rcp_f32_e32 v70, v70
	v_rcp_f32_e32 v68, v68
	v_rcp_f32_e32 v79, v76
	v_rcp_f32_e32 v71, v71
	v_exp_f32_e32 v80, v80
	v_exp_f32_e32 v81, v81
	v_cvt_pk_bf16_f32 v77, v82, v70
	v_cvt_pk_bf16_f32 v78, v68, v78
	v_cvt_pk_bf16_f32 v79, v79, v71
	v_subrev_u32_e32 v68, s16, v72
	v_subrev_u32_e32 v70, s16, v73
	v_subrev_u32_e32 v71, s16, v74
	v_add_f32_e32 v95, 1.0, v95
	v_add_f32_e32 v85, 1.0, v85
	v_add_f32_e32 v80, 1.0, v80
	v_add_f32_e32 v81, 1.0, v81
	v_max3_u32 v68, v68, v70, v71
	v_subrev_u32_e32 v70, s16, v75
	v_rcp_f32_e32 v95, v95
	v_rcp_f32_e32 v85, v85
	v_rcp_f32_e32 v80, v80
	v_rcp_f32_e32 v81, v81
	v_max_u32_e32 v68, v68, v70
	v_cmp_gt_u32_e32 vcc, 16, v68
	s_cmp_eq_u64 vcc, -1
	s_cselect_b64 s[24:25], -1, 0
	s_cmp_lg_u64 vcc, -1
	v_cvt_pk_bf16_f32 v89, v129, v95
	v_cvt_pk_bf16_f32 v84, v92, v84
	v_cvt_pk_bf16_f32 v85, v93, v85
	v_cvt_pk_bf16_f32 v76, v80, v81
	s_cselect_b64 s[26:27], -1, 0
	v_cmp_gt_u32_e64 s[2:3], s55, v73
	v_cmp_gt_u32_e64 s[4:5], s55, v74
	v_cmp_gt_u32_e64 s[6:7], s55, v75
	s_mov_b32 s8, 0
	s_branch .LBB1_14

amdhsa.kernels:
  - .agpr_count:     0
    .args:
      - .actual_access:  read_only
        .address_space:  global
        .offset:         0
        .size:           8
        .value_kind:     global_buffer
      - .actual_access:  read_only
        .address_space:  global
        .offset:         8
        .size:           8
        .value_kind:     global_buffer
      - .actual_access:  read_only
        .address_space:  global
        .offset:         16
        .size:           8
        .value_kind:     global_buffer
      - .actual_access:  read_only
        .address_space:  global
        .offset:         24
        .size:           8
        .value_kind:     global_buffer
      - .actual_access:  read_only
        .address_space:  global
        .offset:         32
        .size:           8
        .value_kind:     global_buffer
      - .actual_access:  read_only
        .address_space:  global
        .offset:         40
        .size:           8
        .value_kind:     global_buffer
      - .actual_access:  read_only
        .address_space:  global
        .offset:         48
        .size:           8
        .value_kind:     global_buffer
      - .actual_access:  read_only
        .address_space:  global
        .offset:         56
        .size:           8
        .value_kind:     global_buffer
      - .address_space:  global
        .offset:         64
        .size:           8
        .value_kind:     global_buffer
      - .offset:         72
        .size:           4
        .value_kind:     hidden_block_count_x
      - .offset:         76
        .size:           4
        .value_kind:     hidden_block_count_y
      - .offset:         80
        .size:           4
        .value_kind:     hidden_block_count_z
      - .offset:         84
        .size:           2
        .value_kind:     hidden_group_size_x
      - .offset:         86
        .size:           2
        .value_kind:     hidden_group_size_y
      - .offset:         88
        .size:           2
        .value_kind:     hidden_group_size_z
      - .offset:         90
        .size:           2
        .value_kind:     hidden_remainder_x
      - .offset:         92
        .size:           2
        .value_kind:     hidden_remainder_y
      - .offset:         94
        .size:           2
        .value_kind:     hidden_remainder_z
      - .offset:         112
        .size:           8
        .value_kind:     hidden_global_offset_x
      - .offset:         120
        .size:           8
        .value_kind:     hidden_global_offset_y
      - .offset:         128
        .size:           8
        .value_kind:     hidden_global_offset_z
      - .offset:         136
        .size:           2
        .value_kind:     hidden_grid_dims
    .group_segment_fixed_size: 256
    .kernarg_segment_align: 8
    .kernarg_segment_size: 328
    .language:       OpenCL C
    .language_version:
      - 2
      - 0
    .max_flat_workgroup_size: 256
    .name:           _Z11prep_kernelPKfS0_S0_S0_S0_S0_S0_PKiPc
    .private_segment_fixed_size: 0
    .sgpr_count:     58
    .sgpr_spill_count: 0
    .symbol:         _Z11prep_kernelPKfS0_S0_S0_S0_S0_S0_PKiPc.kd
    .uniform_work_group_size: 1
    .uses_dynamic_stack: false
    .vgpr_count:     37
    .vgpr_spill_count: 0
    .wavefront_size: 64
  - .agpr_count:     0
    .args:
      - .actual_access:  read_only
        .address_space:  global
        .offset:         0
        .size:           8
        .value_kind:     global_buffer
      - .address_space:  global
        .offset:         8
        .size:           8
        .value_kind:     global_buffer
      - .actual_access:  read_only
        .address_space:  global
        .offset:         16
        .size:           8
        .value_kind:     global_buffer
      - .actual_access:  read_only
        .address_space:  global
        .offset:         24
        .size:           8
        .value_kind:     global_buffer
      - .address_space:  global
        .offset:         32
        .size:           8
        .value_kind:     global_buffer
      - .address_space:  global
        .offset:         40
        .size:           8
        .value_kind:     global_buffer
      - .actual_access:  read_only
        .address_space:  global
        .offset:         48
        .size:           8
        .value_kind:     global_buffer
      - .offset:         56
        .size:           4
        .value_kind:     by_value
      - .offset:         64
        .size:           4
        .value_kind:     hidden_block_count_x
      - .offset:         68
        .size:           4
        .value_kind:     hidden_block_count_y
      - .offset:         72
        .size:           4
        .value_kind:     hidden_block_count_z
      - .offset:         76
        .size:           2
        .value_kind:     hidden_group_size_x
      - .offset:         78
        .size:           2
        .value_kind:     hidden_group_size_y
      - .offset:         80
        .size:           2
        .value_kind:     hidden_group_size_z
      - .offset:         82
        .size:           2
        .value_kind:     hidden_remainder_x
      - .offset:         84
        .size:           2
        .value_kind:     hidden_remainder_y
      - .offset:         86
        .size:           2
        .value_kind:     hidden_remainder_z
      - .offset:         104
        .size:           8
        .value_kind:     hidden_global_offset_x
      - .offset:         112
        .size:           8
        .value_kind:     hidden_global_offset_y
      - .offset:         120
        .size:           8
        .value_kind:     hidden_global_offset_z
      - .offset:         128
        .size:           2
        .value_kind:     hidden_grid_dims
    .group_segment_fixed_size: 135936
    .kernarg_segment_align: 8
    .kernarg_segment_size: 320
    .language:       OpenCL C
    .language_version:
      - 2
      - 0
    .max_flat_workgroup_size: 768
    .name:           _Z11main_kernelPKfPKiPK15HIP_vector_typeIjLj4EES0_PfS7_S2_i
    .private_segment_fixed_size: 0
    .sgpr_count:     66
    .sgpr_spill_count: 0
    .symbol:         _Z11main_kernelPKfPKiPK15HIP_vector_typeIjLj4EES0_PfS7_S2_i.kd
    .uniform_work_group_size: 1
    .uses_dynamic_stack: false
    .vgpr_count:     156
    .vgpr_spill_count: 0
    .wavefront_size: 64
  - .agpr_count:     60
    .args:
      - .actual_access:  read_only
        .address_space:  global
        .offset:         0
        .size:           8
        .value_kind:     global_buffer
      - .actual_access:  read_only
        .address_space:  global
        .offset:         8
        .size:           8
        .value_kind:     global_buffer
      - .actual_access:  read_only
        .address_space:  global
        .offset:         16
        .size:           8
        .value_kind:     global_buffer
      - .actual_access:  read_only
        .address_space:  global
        .offset:         24
        .size:           8
        .value_kind:     global_buffer
      - .actual_access:  read_only
        .address_space:  global
        .offset:         32
        .size:           8
        .value_kind:     global_buffer
      - .actual_access:  read_only
        .address_space:  global
        .offset:         40
        .size:           8
        .value_kind:     global_buffer
      - .actual_access:  read_only
        .address_space:  global
        .offset:         48
        .size:           8
        .value_kind:     global_buffer
      - .actual_access:  read_only
        .address_space:  global
        .offset:         56
        .size:           8
        .value_kind:     global_buffer
      - .address_space:  global
        .offset:         64
        .size:           8
        .value_kind:     global_buffer
    .group_segment_fixed_size: 86272
    .kernarg_segment_align: 8
    .kernarg_segment_size: 72
    .language:       OpenCL C
    .language_version:
      - 2
      - 0
    .max_flat_workgroup_size: 256
    .name:           _Z10enc_kernelPKfS0_PK15HIP_vector_typeIjLj4EES4_S4_S0_S0_S0_Pf
    .private_segment_fixed_size: 0
    .sgpr_count:     24
    .sgpr_spill_count: 0
    .symbol:         _Z10enc_kernelPKfS0_PK15HIP_vector_typeIjLj4EES4_S4_S0_S0_S0_Pf.kd
    .uniform_work_group_size: 1
    .uses_dynamic_stack: false
    .vgpr_count:     176
    .vgpr_spill_count: 0
    .wavefront_size: 64
